# final norm phase: gain vectors loaded once before the row loop, four row pieces issued together (no per-piece store-ack waits)
# speedup vs baseline: 1.0029x; 1.0001x over previous
.LBB0_1918:
	s_mov_b64 s[8:9], s[54:55]
	s_load_dword s4, s[8:9], 0xd4
	v_mov_b32_e32 v0, v235
	v_readlane_b32 s5, v254, 8
	v_readfirstlane_b32 s1, v0
	s_ashr_i32 s1, s1, 6
	s_add_i32 s6, s1, s5
	s_mov_b32 s1, s76
	s_waitcnt lgkmcnt(0)
	s_cmp_ge_i32 s6, s4
	s_cbranch_scc1 .LBB0_1921
	s_ashr_i32 s5, s4, 31
	v_readlane_b32 s24, v255, 20
	s_load_dwordx4 s[40:43], s[8:9], 0xb0
	s_load_dwordx2 s[18:19], s[8:9], 0xc0
	s_lshl_b32 s8, s1, 3
	s_lshl_b64 s[20:21], s[4:5], 11
	v_readlane_b32 s25, v255, 21
	s_mul_hi_u32 s1, s24, s4
	s_mul_i32 s5, s24, s5
	s_add_i32 s1, s1, s5
	s_mul_i32 s5, s25, s4
	s_ashr_i32 s7, s6, 31
	s_add_i32 s1, s1, s5
	s_mul_i32 s5, s24, s4
	s_lshl_b64 s[24:25], s[6:7], 12
	s_add_u32 s5, s5, s24
	s_addc_u32 s1, s1, s25
	v_and_b32_e32 v2, 63, v0
	s_waitcnt lgkmcnt(0)
	s_add_u32 s24, s42, s5
	v_lshlrev_b32_e32 v0, 4, v2
	v_mov_b32_e32 v1, v48
	s_addc_u32 s25, s43, s1
	s_ashr_i32 s9, s8, 31
	s_waitcnt vmcnt(0)
	v_lshl_add_u64 v[4:5], s[40:41], 0, v[0:1]
	v_lshl_add_u64 v[0:1], s[24:25], 0, v[0:1]
	s_lshl_b64 s[38:39], s[8:9], 12
	s_lshl_b64 s[24:25], s[6:7], 11
	s_add_u32 s1, s20, s24
	s_addc_u32 s5, s21, s25
	s_add_u32 s18, s18, s1
	v_lshl_add_u64 v[6:7], v[0:1], 0, s[78:79]
	v_lshlrev_b32_e32 v0, 3, v2
	v_mov_b32_e32 v1, v48
	s_addc_u32 s19, s19, s5
	v_readlane_b32 s24, v255, 30
	v_lshl_add_u64 v[0:1], s[18:19], 0, v[0:1]
	s_mov_b64 s[18:19], 0x18422400
	v_readlane_b32 s25, v255, 31
	v_lshl_add_u64 v[8:9], v[0:1], 0, s[18:19]
	s_lshl_b64 s[40:41], s[8:9], 11
	global_load_dwordx4 v[36:39], v[4:5], off
	global_load_dwordx4 v[40:43], v[4:5], off offset:1024
	global_load_dwordx4 v[44:47], v[4:5], off offset:2048
	global_load_dwordx4 v[50:53], v[4:5], off offset:3072
.LBB0_1920:
	global_load_dwordx2 v[0:1], v[8:9], off offset:-1024
	global_load_dwordx2 v[14:15], v[8:9], off offset:512
	global_load_dwordx2 v[54:55], v[8:9], off offset:-512
	global_load_dwordx2 v[56:57], v[8:9], off
	s_add_i32 s6, s6, s8
	s_cmp_lt_i32 s6, s4
	s_waitcnt vmcnt(3)
	v_lshlrev_b32_e32 v2, 16, v0
	v_and_b32_e32 v3, 0xffff0000, v0
	v_lshlrev_b32_e32 v0, 16, v1
	v_and_b32_e32 v1, 0xffff0000, v1
	v_mul_f32_e32 v10, v1, v1
	v_pk_fma_f32 v[24:25], v[0:1], v[0:1], v[10:11] op_sel_hi:[1,1,0]
	s_waitcnt vmcnt(2)
	v_lshlrev_b32_e32 v13, 16, v14
	v_mov_b32_e32 v30, v24
	v_mov_b32_e32 v31, v13
	s_waitcnt vmcnt(1)
	v_mov_b32_e32 v10, v54
	v_mov_b32_e32 v11, v55
	v_and_b32_e32 v23, 0xffff0000, v11
	v_and_b32_e32 v22, 0xffff0000, v10
	v_lshlrev_b32_e32 v21, 16, v11
	v_lshlrev_b32_e32 v20, 16, v10
	v_pk_mul_f32 v[10:11], v[22:23], v[22:23]
	s_nop 0
	v_pk_fma_f32 v[26:27], v[20:21], v[20:21], v[10:11]
	v_pk_add_f32 v[26:27], v[26:27], v[26:27] op_sel:[0,1] op_sel_hi:[1,0]
	v_lshl_add_u64 v[8:9], v[8:9], 0, s[40:41]
	s_waitcnt vmcnt(0)
	v_mov_b32_e32 v10, v56
	v_mov_b32_e32 v11, v57
	v_lshlrev_b32_e32 v16, 16, v10
	v_and_b32_e32 v17, 0xffff0000, v10
	v_lshlrev_b32_e32 v18, 16, v11
	v_and_b32_e32 v19, 0xffff0000, v11
	v_and_b32_e32 v11, 0xffff0000, v14
	v_mul_f32_e32 v10, v3, v3
	v_pk_fma_f32 v[28:29], v[2:3], v[2:3], v[10:11] op_sel_hi:[1,1,0]
	v_mul_f32_e32 v32, v11, v11
	v_mov_b32_e32 v12, v28
	v_pk_add_f32 v[24:25], v[28:29], v[24:25]
	v_pk_mul_f32 v[28:29], v[12:13], v[30:31]
	v_mov_b32_e32 v27, v32
	v_mov_b32_e32 v25, v29
	v_mul_f32_e32 v10, v17, v17
	v_lshlrev_b32_e32 v14, 16, v15
	v_and_b32_e32 v15, 0xffff0000, v15
	v_pk_add_f32 v[24:25], v[24:25], v[26:27]
	v_pk_fma_f32 v[26:27], v[16:17], v[16:17], v[10:11] op_sel_hi:[1,1,0]
	v_mul_f32_e32 v10, v19, v19
	v_mul_f32_e32 v33, v14, v14
	v_mul_f32_e32 v34, v15, v15
	v_pk_fma_f32 v[28:29], v[18:19], v[18:19], v[10:11] op_sel_hi:[1,1,0]
	v_mov_b32_e32 v27, v33
	v_mov_b32_e32 v29, v34
	v_pk_add_f32 v[26:27], v[26:27], v[28:29]
	s_nop 0
	v_pk_add_f32 v[24:25], v[24:25], v[26:27]
	s_nop 0
	v_add_f32_e32 v10, v24, v25
	s_nop 1
	v_add_f32_dpp v10, v10, v10 quad_perm:[1,0,3,2] row_mask:0xf bank_mask:0xf bound_ctrl:1
	s_nop 1
	v_add_f32_dpp v10, v10, v10 quad_perm:[2,3,0,1] row_mask:0xf bank_mask:0xf bound_ctrl:1
	s_nop 1
	v_add_f32_dpp v10, v10, v10 row_half_mirror row_mask:0xf bank_mask:0xf bound_ctrl:1
	s_nop 1
	v_add_f32_dpp v10, v10, v10 row_mirror row_mask:0xf bank_mask:0xf bound_ctrl:1
	s_nop 0
	v_readlane_b32 s1, v10, 16
	v_readlane_b32 s5, v10, 48
	v_readlane_b32 s18, v10, 0
	v_readlane_b32 s19, v10, 32
	v_mov_b32_e32 v24, s1
	v_mov_b32_e32 v25, s5
	v_pk_add_f32 v[24:25], s[18:19], v[24:25]
	s_nop 0
	v_add_f32_e32 v10, v24, v25
	v_fmamk_f32 v10, v10, 0x3a800000, v237
	v_cmp_gt_f32_e32 vcc, s13, v10
	v_mul_f32_e32 v12, 0x4b800000, v10
	s_nop 0
	v_cndmask_b32_e32 v10, v10, v12, vcc
	v_rsq_f32_e32 v10, v10
	s_nop 0
	v_mul_f32_e32 v12, 0x45800000, v10
	v_cndmask_b32_e32 v12, v10, v12, vcc
	v_pk_mul_f32 v[24:25], v[12:13], v[2:3] op_sel_hi:[0,1]
	v_pk_mul_f32 v[26:27], v[12:13], v[0:1] op_sel_hi:[0,1]
	v_pk_mul_f32 v[18:19], v[12:13], v[18:19] op_sel_hi:[0,1]
	v_pk_mul_f32 v[16:17], v[12:13], v[16:17] op_sel_hi:[0,1]
	v_mov_b32_e32 v10, v13
	v_pk_mul_f32 v[14:15], v[14:15], v[12:13] op_sel_hi:[1,0]
	v_pk_mul_f32 v[10:11], v[10:11], v[12:13] op_sel_hi:[1,0]
	v_pk_mul_f32 v[2:3], v[38:39], v[26:27]
	v_pk_mul_f32 v[0:1], v[36:37], v[24:25]
	global_store_dwordx4 v[6:7], v[0:3], off offset:-2048
	s_nop 1
	v_mov_b32_e32 v0, v21
	v_mov_b32_e32 v1, v23
	v_pk_mul_f32 v[24:25], v[12:13], v[0:1] op_sel_hi:[0,1]
	s_nop 1
	v_mov_b32_e32 v21, v22
	v_pk_mul_f32 v[20:21], v[12:13], v[20:21] op_sel_hi:[0,1]
	v_pk_mul_f32 v[0:1], v[40:41], v[20:21]
	v_pk_mul_f32 v[2:3], v[42:43], v[24:25]
	global_store_dwordx4 v[6:7], v[0:3], off offset:-1024
	s_nop 1
	v_pk_mul_f32 v[0:1], v[44:45], v[16:17]
	v_pk_mul_f32 v[2:3], v[46:47], v[18:19]
	global_store_dwordx4 v[6:7], v[0:3], off
	s_nop 1
	v_pk_mul_f32 v[0:1], v[50:51], v[10:11]
	v_pk_mul_f32 v[2:3], v[52:53], v[14:15]
	global_store_dwordx4 v[6:7], v[0:3], off offset:1024
	v_lshl_add_u64 v[6:7], v[6:7], 0, s[38:39]
	s_cbranch_scc1 .LBB0_1920
